# speedup vs baseline: 1.0153x; 1.0028x over previous
.Lk2_pro:
	s_cmp_le_u32 s22, 16
	s_cselect_b32 s40, s18, 0x18000
	s_add_u32 m0, s40, s35
	s_add_u32 s22, s22, 1
	global_load_lds_dwordx4 v168, s[20:21] nt
	global_load_lds_dwordx4 v168, s[20:21] offset:1024 nt
	s_cmp_le_u32 s22, 16
	s_cselect_b32 s41, 0x4000, 0
	s_add_u32 s20, s20, s41
	s_addc_u32 s21, s21, 0
	s_add_u32 s18, s18, 0x4000
	s_cmp_eq_u32 s18, 0x18000
	s_cselect_b32 s18, 0, s18
	s_cmp_eq_u32 s38, s39
	s_cbranch_scc0 .Lk2_pro_nopsi
	s_add_u32 s14, s14, 1
	s_cmp_eq_u32 s14, 16
	s_cselect_b32 s42, 1, 0
	s_add_u32 s13, s13, s42
	s_cmp_eq_u32 s42, 1
	s_cselect_b32 s14, s13, s14
	s_min_u32 s43, s13, 15
	s_min_u32 s44, s14, 15
	s_lshl_b32 s45, s44, 16
	s_add_u32 s24, s8, s45
	s_addc_u32 s25, s9, 0
	s_add_u32 s26, s24, 0x100000
	s_addc_u32 s27, s25, 0
	s_lshl_b32 s45, s43, 16
	s_add_u32 s28, s8, s45
	s_addc_u32 s29, s9, 0
	s_add_u32 s30, s28, 0x100000
	s_addc_u32 s31, s29, 0
	global_load_dwordx4 v[60:63], v164, s[24:25]
	global_load_dwordx4 v[56:59], v164, s[26:27]
	global_load_dwordx4 v[64:67], v165, s[28:29]
	global_load_dwordx4 v[68:71], v166, s[28:29]
	global_load_dwordx4 v[72:75], v165, s[30:31]
	global_load_dwordx4 v[76:79], v166, s[30:31]
